# half of the expert-weight conversion runs inside the attention loop (16 loads behind the K reads, pack+store behind the O stores, one unit every 4th iteration, staggered by workgroup); phase 2 convert
# speedup vs baseline: 1.0289x; 1.0226x over previous
; #define LAS __attribute__((address_space(3)))
; __device__ __forceinline__ void convert_experts(Frame& F, int lo, int hi) {
;     const int gw = F.vcu * 8 + F.wave, NGW = F.G * 8;
;     LAS unsigned char* scr = F.lds + F.wave * 16384;
;     unsigned char* W1t = WSP(F, WS_W1T, unsigned char); unsigned char* W2t = WSP(F, WS_W2T, unsigned char);
;     const float* weg = F.a->in[I_WEG]; const float* weu = F.a->in[I_WEU]; const float* wed = F.a->in[I_WED];
;     const float* wsg = F.a->in[I_WSG]; const float* wsu = F.a->in[I_WSU]; const float* wsd = F.a->in[I_WSD];
;     ...
;     constexpr int NPAIRS = CONV_ITEMS / 2;
;     (void)lo; (void)hi;
;     ...
;     if (gw < NPAIRS) {
;         const int ns = 2 * ((NPAIRS - gw + NGW - 1) / NGW);
;         int sq = 0, r = CONV_RIDX(0);
;         TItem tc, tn; CONV_DESC(r, tc); tn = tc;
;         int p = 0; bool first = true;
.Lcva_vcu:
	s_lshr_b32 s99, s99, 6
	s_lshl_b32 s101, s101, 3
	s_add_u32 s89, s101, s99
	s_movk_i32 s90, 12
	s_lshr_b32 s32, s89, 3
	s_mov_b32 s95, 0
	s_waitcnt vmcnt(0)
	s_branch .LBB0_304

; #define LAS __attribute__((address_space(3)))
; __device__ __forceinline__ void convert_experts(Frame& F, int lo, int hi) {
;     ...
;     constexpr int NPAIRS = CONV_ITEMS / 2;
;     (void)lo; (void)hi;
; __device__ __forceinline__ void phase_attn(Frame& F) {
;     ...
;         const unsigned qrow = __umul24((unsigned)(128 * cu.n + ql), (unsigned)cu.d);
;         const float c1 = 0.125f * LOG2E;
;         const float nc2 = -__builtin_amdgcn_exp2f(-(float)(cu.h + 1)) * (float)cu.d * LOG2E;
;         const bool first = cu.n == 0;
;         f32x4 St[9];
;         const f32x4 eb = (f32x4){ef[0], ef[1], ef[2], ef[3]} * nc2;
;         float mx = -INFINITY;
;         bf16x8 kf[9][2];
; #pragma unroll
;         for (int T = 0; T < 9; ++T) { LAS unsigned char* ka = kb + (16 * (w + T) + fr) * ATT_ROWB + fq * 16; kf[T][0] = *(LAS bf16x8*)ka; kf[T][1] = *(LAS bf16x8*)(ka + 64); }
.LBB0_304:
	s_mul_i32 s37, s79, 0x12000
	s_add_i32 s85, s37, 0
	s_waitcnt vmcnt(3)
	v_mov_b64_e32 v[48:49], v[4:5]
	v_mov_b64_e32 v[46:47], v[2:3]
	v_mov_b64_e32 v[44:45], v[8:9]
	v_mov_b64_e32 v[42:43], v[6:7]
	s_lshl_b32 s65, 1, s35
	s_waitcnt lgkmcnt(0)
	s_barrier
	s_add_i32 s37, s30, 1
	v_cvt_f32_u32_e32 v54, s37
	v_cvt_f32_u32_e32 v55, s65
	v_add_u32_e32 v110, s85, v82
	v_add_u32_e32 v58, v110, v90
	v_exp_f32_e64 v54, -v54
	v_add_u32_e32 v66, v110, v91
	v_add_u32_e32 v74, v110, v92
	v_add_u32_e32 v111, v110, v93
	v_mul_f32_e32 v79, v55, v54
	ds_read_b128 v[54:57], v58
	ds_read_b128 v[58:61], v58 offset:64
	ds_read_b128 v[62:65], v66
	ds_read_b128 v[66:69], v66 offset:64
	ds_read_b128 v[70:73], v74
	ds_read_b128 v[74:77], v74 offset:64
	ds_read_b128 v[112:115], v111
	ds_read_b128 v[116:119], v111 offset:64
	v_add_u32_e32 v111, v110, v94
	ds_read_b128 v[120:123], v111
	ds_read_b128 v[124:127], v111 offset:64
	v_add_u32_e32 v111, v110, v95
	ds_read_b128 v[128:131], v111
	ds_read_b128 v[132:135], v111 offset:64
	v_add_u32_e32 v111, v110, v96
	ds_read_b128 v[136:139], v111
	ds_read_b128 v[140:143], v111 offset:64
	v_add_u32_e32 v111, v110, v97
	v_add_u32_e32 v110, v110, v98
	ds_read_b128 v[144:147], v111
	ds_read_b128 v[148:151], v111 offset:64
	ds_read_b128 v[152:155], v110
	ds_read_b128 v[156:159], v110 offset:64
	s_and_b32 s98, s32, 3
	s_add_u32 s32, s32, 1
	s_cmp_eq_u32 s98, 0
	s_cbranch_scc0 .Lcva_none_l
	s_cmp_eq_u32 s90, 0
	s_cbranch_scc1 .Lcva_none_l
	s_sub_u32 s90, s90, 1
	s_lshr_b32 s98, s89, 6
	s_and_b32 s99, s89, 63
	s_mul_hi_u32 s100, s98, 0xaaaaaaab
	s_lshr_b32 s100, s100, 1
	s_mul_i32 s101, s100, 3
	s_sub_u32 s101, s98, s101
	s_cmp_lt_u32 s100, 256
	s_cselect_b32 s98, 0, 3
	s_cselect_b32 s95, s100, 0
	s_add_u32 s98, s98, s101
	s_lshl_b32 s98, s98, 1
	v_readlane_b32 s96, v253, s98
	s_add_u32 s98, s98, 1
	v_readlane_b32 s97, v253, s98
	s_lshl_b32 s95, s95, 20
	s_nop 3
	s_add_u32 s96, s96, s95
	s_addc_u32 s97, s97, 0
	s_cmp_eq_u32 s101, 2
	s_cbranch_scc1 .Lcva_down_l
	s_lshr_b32 s95, s99, 3
	s_and_b32 s99, s99, 7
	s_lshl_b32 s98, s95, 17
	s_add_u32 s96, s96, s98
	s_addc_u32 s97, s97, 0
	s_lshl_b32 s98, s99, 7
	s_add_u32 s96, s96, s98
	s_addc_u32 s97, s97, 0
	s_lshl_b32 s100, s100, 19
	s_lshr_b32 s98, s99, 2
	s_lshl_b32 s98, s98, 18
	s_add_u32 s100, s100, s98
	s_and_b32 s98, s99, 3
	s_lshl_b32 s98, s98, 15
	s_add_u32 s100, s100, s98
	s_lshl_b32 s98, s101, 17
	s_add_u32 s100, s100, s98
	s_lshl_b32 s98, s95, 7
	s_add_u32 s100, s100, s98
	v_readlane_b32 s92, v253, 12
	v_readlane_b32 s93, v253, 13
	s_mov_b32 s94, 0xc3317218
	s_cmp_eq_u32 s101, 0
	s_cselect_b32 s94, 0xc2b8aa3b, s94
	s_nop 3
	s_add_u32 s92, s92, s100
	s_addc_u32 s93, s93, 0
	s_movk_i32 s95, 0x400
	s_movk_i32 s98, 0x400
	s_branch .Lcva_go_l

; #define LAS __attribute__((address_space(3)))
; __device__ __forceinline__ void titem_issue(const TItem& t, int lane, LAS unsigned char* buf) {
;     const int nblk = t.N / 32, kb = t.item / nblk, nb = t.item % nblk, k0 = 64 * kb, n0 = 32 * nb;
; #pragma unroll
;     for (int j = 0; j < 8; ++j) { const float* g = t.W + (size_t)(k0 + 8 * j + (lane >> 3)) * t.N + n0 + 4 * ((lane & 7) ^ j);
;         __builtin_amdgcn_global_load_lds((const unsigned*)g, (LAS unsigned*)(buf + j * 1024), 16, 0, 2); }
; }
; __device__ __forceinline__ void phase_attn(Frame& F) {
;     ...
;         for (int T = 0; T < 9; ++T) {
;             f32x4 sa = (f32x4){0.f, 0.f, 0.f, 0.f};
;             sa = __builtin_amdgcn_mfma_f32_16x16x32_bf16(kf[T][0], q0, sa, 0, 0, 0);
;             sa = __builtin_amdgcn_mfma_f32_16x16x32_bf16(kf[T][1], q1, sa, 0, 0, 0);
;             const float kT = (!first || w + T >= 8) ? nc2 * (float)(128 - 16 * T) : -INFINITY;
;             sa = sa * c1 + (eb + kT);
; #pragma unroll
;             for (int rg = 0; rg < 4; ++rg) {
;                 if (T == 0) sa[rg] = ef[rg] <= 0.f ? sa[rg] : -INFINITY;
;                 if (T == 8) sa[rg] = ef[rg] >= 0.f ? sa[rg] : -INFINITY;
;             }
;             St[T] = sa;
;             mx = fmaxf(mx, fmaxf(fmaxf(sa[0], sa[1]), fmaxf(sa[2], sa[3])));
.Lcva_go_l:
	s_lshl_b32 s99, s98, 4
	v_mad_u32_u24 v250, v248, s99, v249
	global_load_dwordx4 v[168:171], v250, s[96:97] nt
	s_add_u32 s96, s96, s98
	s_addc_u32 s97, s97, 0
	global_load_dwordx4 v[172:175], v250, s[96:97] nt
	s_add_u32 s96, s96, s98
	s_addc_u32 s97, s97, 0
	global_load_dwordx4 v[176:179], v250, s[96:97] nt
	s_add_u32 s96, s96, s98
	s_addc_u32 s97, s97, 0
	global_load_dwordx4 v[180:183], v250, s[96:97] nt
	s_add_u32 s96, s96, s98
	s_addc_u32 s97, s97, 0
	global_load_dwordx4 v[184:187], v250, s[96:97] nt
	s_add_u32 s96, s96, s98
	s_addc_u32 s97, s97, 0
	global_load_dwordx4 v[188:191], v250, s[96:97] nt
	s_add_u32 s96, s96, s98
	s_addc_u32 s97, s97, 0
	global_load_dwordx4 v[192:195], v250, s[96:97] nt
	s_add_u32 s96, s96, s98
	s_addc_u32 s97, s97, 0
	global_load_dwordx4 v[196:199], v250, s[96:97] nt
	s_add_u32 s96, s96, s98
	s_addc_u32 s97, s97, 0
	global_load_dwordx4 v[200:203], v250, s[96:97] nt
	s_add_u32 s96, s96, s98
	s_addc_u32 s97, s97, 0
	global_load_dwordx4 v[204:207], v250, s[96:97] nt
	s_add_u32 s96, s96, s98
	s_addc_u32 s97, s97, 0
	global_load_dwordx4 v[208:211], v250, s[96:97] nt
	s_add_u32 s96, s96, s98
	s_addc_u32 s97, s97, 0
	global_load_dwordx4 v[212:215], v250, s[96:97] nt
	s_add_u32 s96, s96, s98
	s_addc_u32 s97, s97, 0
	global_load_dwordx4 v[216:219], v250, s[96:97] nt
	s_add_u32 s96, s96, s98
	s_addc_u32 s97, s97, 0
	global_load_dwordx4 v[220:223], v250, s[96:97] nt
	s_add_u32 s96, s96, s98
	s_addc_u32 s97, s97, 0
	global_load_dwordx4 v[224:227], v250, s[96:97] nt
	s_add_u32 s96, s96, s98
	s_addc_u32 s97, s97, 0
	global_load_dwordx4 v[228:231], v250, s[96:97] nt
	s_lshl_b32 s99, s69, 6
	s_add_u32 s89, s89, s99
.Lcva_none_l:
	s_cmp_lg_u32 s64, 0
	v_lshl_add_u32 v78, s64, 7, v86
	s_cselect_b64 s[64:65], -1, 0
	v_mul_f32_e32 v160, 0xbfb8aa3b, v79
	v_and_b32_e32 v110, 0xffffff, v78
	s_waitcnt lgkmcnt(14)
	v_mfma_f32_16x16x32_bf16 v[54:57], v[54:57], v[46:49], 0
	v_mul_f32_e32 v78, 0x43000000, v160
	s_or_b64 vcc, s[64:65], s[38:39]
	v_cndmask_b32_e32 v78, v109, v78, vcc
	v_mfma_f32_16x16x32_bf16 v[54:57], v[58:61], v[42:45], v[54:57]
	v_fma_f32 v162, v50, v160, v78
	v_fma_f32 v163, v51, v160, v78
	v_pk_fma_f32 v[78:79], v[52:53], v[160:161], v[78:79] op_sel_hi:[1,0,0]
	s_or_b64 vcc, s[64:65], s[40:41]
	s_nop 3
	v_pk_fma_f32 v[56:57], v[56:57], s[56:57], v[78:79] op_sel_hi:[1,0,1]
	v_pk_fma_f32 v[54:55], v[54:55], s[56:57], v[162:163] op_sel_hi:[1,0,1]
	v_cndmask_b32_e64 v164, v109, v56, s[10:11]
	v_cndmask_b32_e64 v162, v109, v54, s[6:7]
	v_cndmask_b32_e64 v163, v109, v55, s[8:9]
	v_cndmask_b32_e64 v165, v109, v57, s[12:13]
	v_mfma_f32_16x16x32_bf16 v[54:57], v[62:65], v[46:49], 0
	v_max_f32_e32 v58, v162, v163
	v_max_f32_e32 v59, v164, v165
	v_max3_f32 v62, v58, v59, s78
	v_mfma_f32_16x16x32_bf16 v[54:57], v[66:69], v[42:45], v[54:57]
	v_mul_f32_e32 v58, 0x42e00000, v160
	v_cndmask_b32_e32 v58, v109, v58, vcc
	v_pk_fma_f32 v[60:61], v[50:51], v[160:161], v[58:59] op_sel_hi:[1,0,0]
	v_pk_fma_f32 v[58:59], v[52:53], v[160:161], v[58:59] op_sel_hi:[1,0,0]
	s_or_b64 vcc, s[64:65], s[42:43]
	s_nop 2
	v_pk_fma_f32 v[166:167], v[56:57], s[56:57], v[58:59] op_sel_hi:[1,0,1]
	s_waitcnt lgkmcnt(13)
	v_mfma_f32_16x16x32_bf16 v[56:59], v[70:73], v[46:49], 0
	v_fma_f32 v78, v54, s56, v60
	v_fma_f32 v79, v55, s56, v61
	v_max_f32_e32 v54, v166, v167
	v_max3_f32 v63, v78, v79, v54
	s_waitcnt lgkmcnt(12)
	v_mfma_f32_16x16x32_bf16 v[54:57], v[74:77], v[42:45], v[56:59]
	s_nop 2
	v_mul_f32_e32 v58, 0x42c00000, v160
	v_cndmask_b32_e32 v58, v109, v58, vcc
	v_pk_fma_f32 v[60:61], v[50:51], v[160:161], v[58:59] op_sel_hi:[1,0,0]
	v_pk_fma_f32 v[58:59], v[52:53], v[160:161], v[58:59] op_sel_hi:[1,0,0]
	s_nop 0
	v_pk_fma_f32 v[76:77], v[54:55], s[56:57], v[60:61] op_sel_hi:[1,0,1]
	v_pk_fma_f32 v[74:75], v[56:57], s[56:57], v[58:59] op_sel_hi:[1,0,1]
	s_waitcnt lgkmcnt(11)
	v_mfma_f32_16x16x32_bf16 v[54:57], v[112:115], v[46:49], 0
	v_max_f32_e32 v58, v74, v75
	v_max3_f32 v58, v76, v77, v58
	v_max3_f32 v62, v62, v63, v58
	s_waitcnt lgkmcnt(10)
	v_mfma_f32_16x16x32_bf16 v[54:57], v[116:119], v[42:45], v[54:57]
	v_mul_f32_e32 v58, 0x42a00000, v160
	s_or_b64 vcc, s[64:65], s[44:45]
	v_cndmask_b32_e32 v58, v109, v58, vcc
	v_pk_fma_f32 v[60:61], v[50:51], v[160:161], v[58:59] op_sel_hi:[1,0,0]
	v_pk_fma_f32 v[58:59], v[52:53], v[160:161], v[58:59] op_sel_hi:[1,0,0]
	s_nop 2
	v_pk_fma_f32 v[72:73], v[54:55], s[56:57], v[60:61] op_sel_hi:[1,0,1]
	v_pk_fma_f32 v[70:71], v[56:57], s[56:57], v[58:59] op_sel_hi:[1,0,1]
	s_waitcnt lgkmcnt(9)
	v_mfma_f32_16x16x32_bf16 v[56:59], v[120:123], v[46:49], 0
	v_max_f32_e32 v54, v70, v71
	v_max3_f32 v63, v72, v73, v54
	s_or_b64 vcc, s[64:65], s[46:47]
	s_waitcnt lgkmcnt(8)
	v_mfma_f32_16x16x32_bf16 v[54:57], v[124:127], v[42:45], v[56:59]
	s_nop 2
	v_mul_f32_e32 v58, 0x42800000, v160
	v_cndmask_b32_e32 v58, v109, v58, vcc
	v_pk_fma_f32 v[60:61], v[50:51], v[160:161], v[58:59] op_sel_hi:[1,0,0]
	v_pk_fma_f32 v[58:59], v[52:53], v[160:161], v[58:59] op_sel_hi:[1,0,0]
	s_nop 0
	v_pk_fma_f32 v[68:69], v[54:55], s[56:57], v[60:61] op_sel_hi:[1,0,1]
	v_pk_fma_f32 v[66:67], v[56:57], s[56:57], v[58:59] op_sel_hi:[1,0,1]
	s_waitcnt lgkmcnt(7)
	v_mfma_f32_16x16x32_bf16 v[54:57], v[128:131], v[46:49], 0
	v_max_f32_e32 v58, v66, v67
	v_max3_f32 v58, v68, v69, v58
	v_max3_f32 v111, v62, v63, v58
	s_waitcnt lgkmcnt(6)
	v_mfma_f32_16x16x32_bf16 v[54:57], v[132:135], v[42:45], v[54:57]
	v_mul_f32_e32 v58, 0x42400000, v160
	s_or_b64 vcc, s[64:65], s[48:49]
	v_cndmask_b32_e32 v58, v109, v58, vcc
	v_pk_fma_f32 v[60:61], v[50:51], v[160:161], v[58:59] op_sel_hi:[1,0,0]
	v_pk_fma_f32 v[58:59], v[52:53], v[160:161], v[58:59] op_sel_hi:[1,0,0]
	s_nop 2
	v_pk_fma_f32 v[64:65], v[54:55], s[56:57], v[60:61] op_sel_hi:[1,0,1]
	v_pk_fma_f32 v[62:63], v[56:57], s[56:57], v[58:59] op_sel_hi:[1,0,1]
	s_waitcnt lgkmcnt(5)
; #define LAS __attribute__((address_space(3)))
; __device__ __forceinline__ void phase_attn(Frame& F) {
;     ...
;             LAS unsigned char* ob = F.lds + (buf ^ 1) * ABUF;
; #pragma unroll
;             for (int jj = 0; jj < 4; ++jj) { const int ch = tid + 512 * jj, row = ch >> 3, c16 = ch & 7;
;                 *(LAS u32x4*)(ob + row * ATT_ROWB + c16 * 16) = kr[jj]; *(LAS u32x4*)(ob + ATT_VOFF + row * ATT_ROWB + c16 * 16) = vr[jj]; }
;         }
;         const AttnUnit nu = un;
;         un = attn_decode(x8 * PER_X + (jl + 2 * G8 < jlast ? jl + 2 * G8 : jlast)); attn_issue(qkv, un, tid, kr, vr);
;         { const char* qb = (const char*)qkv + (((size_t)nu.b * SEQ + nu.r) * NPROJ + nu.h * 64) * 2; const unsigned qo = __umul24((unsigned)(128 * nu.n + ql), (unsigned)nu.d * (NPROJ * 2)) + 16u * fq;
;           qn0 = *(const bf16x8*)(qb + qo); qn1 = *(const bf16x8*)(qb + qo + 64); }
;     ...
;         for (int T = 0; T < 9; ++T) {
;             f32x4 sa = (f32x4){0.f, 0.f, 0.f, 0.f};
;             sa = __builtin_amdgcn_mfma_f32_16x16x32_bf16(kf[T][0], q0, sa, 0, 0, 0);
;             sa = __builtin_amdgcn_mfma_f32_16x16x32_bf16(kf[T][1], q1, sa, 0, 0, 0);
;             const float kT = (!first || w + T >= 8) ? nc2 * (float)(128 - 16 * T) : -INFINITY;
;             sa = sa * c1 + (eb + kT);
; #pragma unroll
;             for (int rg = 0; rg < 4; ++rg) {
;                 if (T == 0) sa[rg] = ef[rg] <= 0.f ? sa[rg] : -INFINITY;
;                 if (T == 8) sa[rg] = ef[rg] >= 0.f ? sa[rg] : -INFINITY;
;             }
;             St[T] = sa;
;             mx = fmaxf(mx, fmaxf(fmaxf(sa[0], sa[1]), fmaxf(sa[2], sa[3])));
;         }
;         mx = fmaxf(mx, __shfl_xor(mx, 16)); mx = fmaxf(mx, __shfl_xor(mx, 32));
	v_mfma_f32_16x16x32_bf16 v[56:59], v[136:139], v[46:49], 0
	v_max_f32_e32 v54, v62, v63
	v_max3_f32 v112, v64, v65, v54
	s_or_b64 vcc, s[64:65], s[50:51]
	s_waitcnt lgkmcnt(4)
	v_mfma_f32_16x16x32_bf16 v[54:57], v[140:143], v[42:45], v[56:59]
	s_nop 2
	v_mul_f32_e32 v58, 0x42000000, v160
	v_cndmask_b32_e32 v58, v109, v58, vcc
	v_pk_fma_f32 v[60:61], v[50:51], v[160:161], v[58:59] op_sel_hi:[1,0,0]
	v_pk_fma_f32 v[58:59], v[52:53], v[160:161], v[58:59] op_sel_hi:[1,0,0]
	s_nop 0
	v_pk_fma_f32 v[60:61], v[54:55], s[56:57], v[60:61] op_sel_hi:[1,0,1]
	v_pk_fma_f32 v[58:59], v[56:57], s[56:57], v[58:59] op_sel_hi:[1,0,1]
	s_waitcnt lgkmcnt(3)
	v_mfma_f32_16x16x32_bf16 v[54:57], v[144:147], v[46:49], 0
	v_max_f32_e32 v113, v58, v59
	v_max3_f32 v113, v60, v61, v113
	v_max3_f32 v111, v111, v112, v113
	s_waitcnt lgkmcnt(1)
	v_mfma_f32_16x16x32_bf16 v[46:49], v[152:155], v[46:49], 0
	s_or_b64 vcc, s[64:65], s[52:53]
	v_add_u32_e32 v144, s85, v89
	v_add_u32_e32 v130, v144, v99
	v_mfma_f32_16x16x32_bf16 v[112:115], v[148:151], v[42:45], v[54:57]
	v_add_u32_e32 v140, v144, v100
	v_add_u32_e32 v145, v144, v101
	s_nop 0
	v_mul_f32_e32 v54, 0x41800000, v160
	s_waitcnt lgkmcnt(0)
	v_mfma_f32_16x16x32_bf16 v[42:45], v[156:159], v[42:45], v[46:49]
	s_add_i32 s37, s77, s70
	s_xor_b32 s79, s79, 1
	s_min_i32 s37, s37, s71
	s_mul_i32 s58, s79, 0x12000
	s_add_i32 s37, s37, s3
	v_add_u32_e32 v2, s58, v84
	s_mul_hi_i32 s58, s37, 0x2aaaaaab
	s_lshr_b32 s59, s58, 31
	s_ashr_i32 s58, s58, 4
	s_add_i32 s59, s58, s59
	s_mul_i32 s58, s59, 0x60
	s_sub_i32 s37, s37, s58
	s_ashr_i32 s58, s59, 3
	s_and_b32 s80, s59, 7
	v_add_u32_e32 v3, v2, v83
	s_cmp_gt_i32 s37, 31
	ds_write_b128 v3, v[38:41]
	ds_write_b128 v3, v[34:37] offset:36864
	v_add_u32_e32 v3, v2, v85
	s_cselect_b64 s[82:83], -1, 0
	s_cmp_gt_i32 s37, 63
	ds_write_b128 v3, v[30:33]
	ds_write_b128 v3, v[26:29] offset:36864
	v_add_u32_e32 v3, v2, v87
	v_add_u32_e32 v2, v2, v88
	s_cselect_b64 s[86:87], -1, 0
	ds_write_b128 v3, v[22:25]
	ds_write_b128 v3, v[18:21] offset:36864
	ds_write_b128 v2, v[14:17]
	ds_write_b128 v2, v[10:13] offset:36864
	v_cndmask_b32_e64 v2, 0, 1, s[86:87]
	s_cmp_lg_u64 s[82:83], 0
	v_readfirstlane_b32 s59, v2
	s_addc_u32 s81, s59, 0
	s_lshl_b32 s59, s81, 5
	s_lshl_b32 s82, s81, 1
	s_sub_i32 s37, s37, s59
	s_sub_i32 s59, 5, s82
	s_ashr_i32 s83, s37, s59
	s_lshl_b32 s59, -1, s59
	s_andn2_b32 s84, s37, s59
	s_ashr_i32 s59, s58, 31
	s_lshl_b64 s[86:87], s[58:59], 12
	s_ashr_i32 s37, s83, 31
	s_add_u32 s59, s86, s83
	s_addc_u32 s37, s87, s37
	s_mulk_i32 s37, 0xa00
	s_mul_hi_u32 s86, s59, 0xa00
	s_add_i32 s87, s86, s37
	s_mulk_i32 s59, 0xa00
	s_lshl_b32 s37, s80, 6
	s_or_b32 s86, s59, s37
	s_lshl_b64 s[86:87], s[86:87], 1
	s_add_u32 s37, s33, s86
	s_addc_u32 s59, s66, s87
	s_add_u32 s86, s37, 0x400
	s_addc_u32 s87, s59, 0
	s_lshl_b32 s59, s84, 7
	v_add_u32_e32 v2, s59, v81
	s_lshl_b32 s37, 0x1400, s82
	v_max_i32_e32 v3, 0, v2
	v_mul_u32_u24_e32 v3, s37, v3
	v_or_b32_e32 v3, v3, v80
	global_load_dwordx4 v[38:41], v3, s[86:87]
	global_load_dwordx4 v[34:37], v3, s[86:87] offset:1024
	v_max_i32_e32 v3, 0xffffffc0, v2
	v_add_u32_e32 v3, 64, v3
	v_mul_u32_u24_e32 v3, s37, v3
	v_or_b32_e32 v3, v3, v80
	global_load_dwordx4 v[30:33], v3, s[86:87]
	global_load_dwordx4 v[26:29], v3, s[86:87] offset:1024
	v_add_u32_e32 v3, s59, v1
	v_max_i32_e32 v2, 0xffffff40, v2
	v_max_i32_e32 v3, 0, v3
	v_add_u32_e32 v2, 0xc0, v2
	v_mul_u32_u24_e32 v3, s37, v3
	v_mul_u32_u24_e32 v2, s37, v2
	v_or_b32_e32 v3, v3, v80
	v_or_b32_e32 v2, v2, v80
	s_ashr_i32 s37, s36, 31
	global_load_dwordx4 v[22:25], v3, s[86:87]
	global_load_dwordx4 v[18:21], v3, s[86:87] offset:1024
	global_load_dwordx4 v[14:17], v2, s[86:87]
	global_load_dwordx4 v[10:13], v2, s[86:87] offset:1024
	s_lshl_b64 s[86:87], s[36:37], 12
	s_ashr_i32 s37, s73, 31
	s_add_u32 s59, s86, s73
	s_addc_u32 s37, s87, s37
	s_mulk_i32 s37, 0xa00
	s_mul_hi_u32 s86, s59, 0xa00
	s_add_i32 s87, s86, s37
	s_mulk_i32 s59, 0xa00
	s_lshl_b32 s37, s75, 6
	s_or_b32 s86, s59, s37
	s_lshl_b64 s[86:87], s[86:87], 1
	s_add_u32 s86, s33, s86
	s_addc_u32 s87, s66, s87
	s_lshl_b32 s37, 0x1400, s74
	v_lshl_add_u32 v2, s76, 7, v86
	s_and_b32 s37, s37, 0x555400
	v_mul_u32_u24_e32 v2, s37, v2
	v_or_b32_e32 v6, v2, v82
	global_load_dwordx4 v[2:5], v6, s[86:87]
	s_nop 0
	global_load_dwordx4 v[6:9], v6, s[86:87] offset:64
	v_cndmask_b32_e32 v54, v109, v54, vcc
	s_or_b64 vcc, s[64:65], s[54:55]
	v_pk_fma_f32 v[56:57], v[50:51], v[160:161], v[54:55] op_sel_hi:[1,0,0]
	v_mul_f32_e32 v46, 0, v160
	v_cndmask_b32_e32 v46, v109, v46, vcc
	v_pk_fma_f32 v[48:49], v[50:51], v[160:161], v[46:47] op_sel_hi:[1,0,0]
	v_pk_fma_f32 v[46:47], v[52:53], v[160:161], v[46:47] op_sel_hi:[1,0,0]
	v_pk_fma_f32 v[54:55], v[52:53], v[160:161], v[54:55] op_sel_hi:[1,0,0]
	v_pk_fma_f32 v[44:45], v[44:45], s[56:57], v[46:47] op_sel_hi:[1,0,1]
	v_pk_fma_f32 v[42:43], v[42:43], s[56:57], v[48:49] op_sel_hi:[1,0,1]
	v_cndmask_b32_e64 v48, v109, v44, s[18:19]
	v_and_b32_e32 v44, 64, v108
	v_pk_fma_f32 v[54:55], v[114:115], s[56:57], v[54:55] op_sel_hi:[1,0,1]
	v_cndmask_b32_e64 v47, v109, v43, s[16:17]
	v_cndmask_b32_e64 v49, v109, v45, s[20:21]
	v_xor_b32_e32 v43, 16, v108
	v_add_u32_e32 v44, 64, v44
	v_pk_fma_f32 v[56:57], v[112:113], s[56:57], v[56:57] op_sel_hi:[1,0,1]
	v_max_f32_e32 v112, v54, v55
	v_cndmask_b32_e64 v46, v109, v42, s[14:15]
	v_max_f32_e32 v42, v48, v49
	v_cmp_lt_i32_e32 vcc, v43, v44
	v_max3_f32 v112, v56, v57, v112
	v_max3_f32 v42, v46, v47, v42
	v_cndmask_b32_e32 v43, v108, v43, vcc
	v_max3_f32 v42, v111, v112, v42
	v_lshlrev_b32_e32 v142, 2, v43
	ds_bpermute_b32 v43, v142, v42
	s_waitcnt lgkmcnt(0)
; #define LAS __attribute__((address_space(3)))
; __device__ __forceinline__ unsigned cvt_pk_bf16(float lo, float hi) { const f32x2_t v = {lo, hi}; return __builtin_bit_cast(unsigned, __builtin_convertvector(v, bf16x2_t)); }
; __device__ __forceinline__ float fast_exp2(float x) { return __builtin_amdgcn_exp2f(x); }
; __device__ __forceinline__ s16x4 tr_read(LAS unsigned char* p) { return __builtin_bit_cast(s16x4, __builtin_amdgcn_ds_read_tr16_b64_v4i16((LAS s16x4*)p)); }
; __device__ __forceinline__ void phase_attn(Frame& F) {
;     ...
;         mx = fmaxf(mx, __shfl_xor(mx, 16)); mx = fmaxf(mx, __shfl_xor(mx, 32));
;         f32x4 lv = (f32x4){0.f, 0.f, 0.f, 0.f};
;         f32x4 nmx = (f32x4){-mx, -mx, -mx, -mx}; asm volatile("" : "+v"(nmx));
; #pragma unroll
;         for (int T = 0; T < 9; ++T) { const f32x4 d = St[T] + nmx; f32x4 pv; pv.x = fast_exp2(d.x); pv.y = fast_exp2(d.y); pv.z = fast_exp2(d.z); pv.w = fast_exp2(d.w); St[T] = pv; lv = lv + pv; }
;         float l = (lv.x + lv.y) + (lv.z + lv.w);
;         l += __shfl_xor(l, 16); l += __shfl_xor(l, 32);
;         f32x4 O[4];
; #pragma unroll
;         for (int dt = 0; dt < 4; ++dt) O[dt] = (f32x4){0.f, 0.f, 0.f, 0.f};
; #pragma unroll
;         for (int T = 0; T < 9; ++T) {
;             u32x2 pw; pw.x = cvt_pk_bf16(St[T][0], St[T][1]); pw.y = cvt_pk_bf16(St[T][2], St[T][3]);
;             const s16x4 pb = __builtin_bit_cast(s16x4, pw);
;             LAS unsigned char* va = kb + ATT_VOFF + (16 * (w + T) + 4 * fq + (fr >> 2)) * ATT_ROWB + (8 * (fr & 3)) * 2;
; #pragma unroll
;             for (int dt = 0; dt < 4; ++dt) O[dt] = __builtin_amdgcn_mfma_f32_16x16x16bf16_1k(tr_read(va + 64 * (dt >> 1) + 8 * (dt & 1)), pb, O[dt], 0, 0, 0);
	v_max_f32_e32 v43, v43, v43
	v_max_f32_e32 v42, v42, v43
	v_xor_b32_e32 v43, 32, v108
	v_cmp_lt_i32_e32 vcc, v43, v44
	s_nop 1
	v_cndmask_b32_e32 v43, v108, v43, vcc
	v_lshlrev_b32_e32 v143, 2, v43
	ds_bpermute_b32 v43, v143, v42
	s_waitcnt lgkmcnt(0)
	v_max_f32_e32 v43, v43, v43
	v_max_f32_e32 v111, v42, v43
	v_xor_b32_e32 v42, 0x80000000, v111
	v_mov_b32_e32 v43, v42
	v_mov_b32_e32 v44, v42
	v_mov_b32_e32 v45, v42
	ds_read_b64_tr_b16 v[120:121], v130 offset:36864
	v_pk_add_f32 v[118:119], v[166:167], v[44:45]
	v_pk_add_f32 v[112:113], v[164:165], v[44:45]
	v_exp_f32_e32 v126, v118
	v_exp_f32_e32 v127, v119
	ds_read_b64_tr_b16 v[118:119], v130 offset:36872
	v_pk_add_f32 v[114:115], v[162:163], v[42:43]
	v_exp_f32_e32 v112, v112
	v_exp_f32_e32 v114, v114
	v_exp_f32_e32 v113, v113
	v_exp_f32_e32 v115, v115
	ds_read_b64_tr_b16 v[128:129], v130 offset:36928
	ds_read_b64_tr_b16 v[130:131], v130 offset:36936
	v_pk_add_f32 v[134:135], v[76:77], v[42:43]
	v_cvt_pk_bf16_f32 v123, v112, v113
	v_cvt_pk_bf16_f32 v122, v114, v115
	v_pk_add_f32 v[116:117], v[112:113], 0 op_sel_hi:[1,0]
	v_pk_add_f32 v[124:125], v[114:115], 0 op_sel_hi:[1,0]
	s_waitcnt lgkmcnt(3)
	v_mfma_f32_16x16x16_bf16 v[112:115], v[120:121], v[122:123], 0
	v_add_f32_e64 v120, v74, v44
	v_add_f32_e64 v121, v75, v45
	v_pk_add_f32 v[132:133], v[126:127], v[116:117]
	v_exp_f32_e32 v136, v120
	s_waitcnt lgkmcnt(2)
	v_mfma_f32_16x16x16_bf16 v[116:119], v[118:119], v[122:123], 0
	v_exp_f32_e32 v137, v121
	v_pk_add_f32 v[78:79], v[78:79], v[42:43]
	v_cvt_pk_bf16_f32 v139, v126, v127
	s_waitcnt lgkmcnt(1)
	v_mfma_f32_16x16x16_bf16 v[74:77], v[128:129], v[122:123], 0
	ds_read_b64_tr_b16 v[128:129], v140 offset:36864
	v_exp_f32_e32 v78, v78
	v_exp_f32_e32 v79, v79
	s_waitcnt lgkmcnt(1)
	v_mfma_f32_16x16x16_bf16 v[120:123], v[130:131], v[122:123], 0
	ds_read_b64_tr_b16 v[130:131], v140 offset:36872
	ds_read_b64_tr_b16 v[126:127], v140 offset:36928
	ds_read_b64_tr_b16 v[140:141], v140 offset:36936
	v_cvt_pk_bf16_f32 v138, v78, v79
	v_exp_f32_e32 v134, v134
	v_exp_f32_e32 v135, v135
	s_waitcnt lgkmcnt(3)
	v_mfma_f32_16x16x16_bf16 v[112:115], v[128:129], v[138:139], v[112:115]
	v_add_f32_e64 v128, v70, v44
	v_add_f32_e64 v129, v71, v45
	v_pk_add_f32 v[78:79], v[78:79], v[124:125]
	v_pk_add_f32 v[124:125], v[136:137], v[132:133]
	s_waitcnt lgkmcnt(2)
	v_mfma_f32_16x16x16_bf16 v[116:119], v[130:131], v[138:139], v[116:119]
	v_add_f32_e64 v130, v72, v42
	v_add_f32_e64 v131, v73, v43
	v_pk_add_f32 v[78:79], v[134:135], v[78:79]
	v_exp_f32_e32 v128, v128
	s_waitcnt lgkmcnt(1)
	v_mfma_f32_16x16x16_bf16 v[70:73], v[126:127], v[138:139], v[74:77]
	ds_read_b64_tr_b16 v[126:127], v145 offset:36864
	v_exp_f32_e32 v129, v129
	v_pk_add_f32 v[48:49], v[44:45], v[48:49]
	s_waitcnt lgkmcnt(1)
	v_mfma_f32_16x16x16_bf16 v[74:77], v[140:141], v[138:139], v[120:123]
	v_add_f32_e64 v124, v128, v124
	v_add_f32_e64 v125, v129, v125
	s_nop 0
	ds_read_b64_tr_b16 v[120:121], v145 offset:36872
	v_cvt_pk_bf16_f32 v122, v134, v135
	ds_read_b64_tr_b16 v[132:133], v145 offset:36928
	ds_read_b64_tr_b16 v[134:135], v145 offset:36936
	v_cvt_pk_bf16_f32 v123, v136, v137
	v_add_u32_e32 v136, v144, v102
	s_waitcnt lgkmcnt(3)
	v_mfma_f32_16x16x16_bf16 v[112:115], v[126:127], v[122:123], v[112:115]
	v_exp_f32_e32 v126, v130
	v_exp_f32_e32 v127, v131
	v_pk_add_f32 v[130:131], v[68:69], v[42:43]
	s_waitcnt lgkmcnt(2)
	v_mfma_f32_16x16x16_bf16 v[116:119], v[120:121], v[122:123], v[116:119]
	v_add_f32_e64 v120, v66, v44
	v_add_f32_e64 v121, v67, v45
	v_pk_add_f32 v[78:79], v[126:127], v[78:79]
	v_exp_f32_e32 v130, v130
	s_waitcnt lgkmcnt(1)
	v_mfma_f32_16x16x16_bf16 v[66:69], v[132:133], v[122:123], v[70:73]
	ds_read_b64_tr_b16 v[132:133], v136 offset:36864
	v_exp_f32_e32 v120, v120
	v_exp_f32_e32 v121, v121
	s_waitcnt lgkmcnt(1)
	v_mfma_f32_16x16x16_bf16 v[70:73], v[134:135], v[122:123], v[74:77]
	ds_read_b64_tr_b16 v[122:123], v136 offset:36872
	v_cvt_pk_bf16_f32 v134, v126, v127
	v_cvt_pk_bf16_f32 v135, v128, v129
	ds_read_b64_tr_b16 v[128:129], v136 offset:36928
	ds_read_b64_tr_b16 v[136:137], v136 offset:36936
	s_waitcnt lgkmcnt(3)
	v_mfma_f32_16x16x16_bf16 v[74:77], v[132:133], v[134:135], v[112:115]
	v_add_u32_e32 v132, v144, v103
	ds_read_b64_tr_b16 v[126:127], v132 offset:36872
	v_exp_f32_e32 v131, v131
	s_waitcnt lgkmcnt(3)
	v_mfma_f32_16x16x16_bf16 v[112:115], v[122:123], v[134:135], v[116:119]
	ds_read_b64_tr_b16 v[122:123], v132 offset:36864
	v_pk_add_f32 v[124:125], v[120:121], v[124:125]
	v_pk_add_f32 v[78:79], v[130:131], v[78:79]
	v_pk_add_f32 v[116:117], v[62:63], v[44:45]
	v_pk_add_f32 v[118:119], v[64:65], v[42:43]
	s_waitcnt lgkmcnt(3)
	v_mfma_f32_16x16x16_bf16 v[62:65], v[128:129], v[134:135], v[66:69]
	v_exp_f32_e32 v116, v116
	v_exp_f32_e32 v117, v117
	v_cvt_pk_bf16_f32 v128, v130, v131
	v_cvt_pk_bf16_f32 v129, v120, v121
	ds_read_b64_tr_b16 v[120:121], v132 offset:36928
	ds_read_b64_tr_b16 v[130:131], v132 offset:36936
	v_add_u32_e32 v132, v144, v104
	s_waitcnt lgkmcnt(4)
	v_mfma_f32_16x16x16_bf16 v[66:69], v[136:137], v[134:135], v[70:73]
	v_exp_f32_e32 v118, v118
	v_exp_f32_e32 v119, v119
	s_waitcnt lgkmcnt(2)
	v_mfma_f32_16x16x16_bf16 v[70:73], v[122:123], v[128:129], v[74:77]
	v_add_f32_e64 v122, v116, v124
	v_add_f32_e64 v123, v117, v125
	ds_read_b64_tr_b16 v[124:125], v132 offset:36872
	v_pk_add_f32 v[78:79], v[118:119], v[78:79]
	v_mfma_f32_16x16x16_bf16 v[74:77], v[126:127], v[128:129], v[112:115]
	v_cvt_pk_bf16_f32 v127, v116, v117
	v_cvt_pk_bf16_f32 v126, v118, v119
	s_nop 0
	v_pk_add_f32 v[112:113], v[58:59], v[44:45]
	v_pk_add_f32 v[114:115], v[60:61], v[42:43]
	s_waitcnt lgkmcnt(2)
; #define LAS __attribute__((address_space(3)))
; __device__ __forceinline__ unsigned cvt_pk_bf16(float lo, float hi) { const f32x2_t v = {lo, hi}; return __builtin_bit_cast(unsigned, __builtin_convertvector(v, bf16x2_t)); }
; __device__ __forceinline__ s16x4 tr_read(LAS unsigned char* p) { return __builtin_bit_cast(s16x4, __builtin_amdgcn_ds_read_tr16_b64_v4i16((LAS s16x4*)p)); }
; __device__ __forceinline__ void phase_attn(Frame& F) {
;     ...
;         for (int T = 0; T < 9; ++T) {
;             u32x2 pw; pw.x = cvt_pk_bf16(St[T][0], St[T][1]); pw.y = cvt_pk_bf16(St[T][2], St[T][3]);
;             const s16x4 pb = __builtin_bit_cast(s16x4, pw);
;             LAS unsigned char* va = kb + ATT_VOFF + (16 * (w + T) + 4 * fq + (fr >> 2)) * ATT_ROWB + (8 * (fr & 3)) * 2;
; #pragma unroll
;             for (int dt = 0; dt < 4; ++dt) O[dt] = __builtin_amdgcn_mfma_f32_16x16x16bf16_1k(tr_read(va + 64 * (dt >> 1) + 8 * (dt & 1)), pb, O[dt], 0, 0, 0);
;         }
;         const float inv = 1.f / l;
;         bf16_t* op = (bf16_t*)((char*)part + (((size_t)cu.dsel * NTOK + (size_t)cu.b * SEQ + cu.r) * 512 + cu.h * 64) * 2 + (qrow * 1024u + 16u * fq));
; #pragma unroll
;         for (int u2 = 0; u2 < 2; ++u2) { u32x4 o4; o4.x = cvt_pk_bf16(O[2 * u2][0] * inv, O[2 * u2][1] * inv); o4.y = cvt_pk_bf16(O[2 * u2][2] * inv, O[2 * u2][3] * inv);
;             o4.z = cvt_pk_bf16(O[2 * u2 + 1][0] * inv, O[2 * u2 + 1][1] * inv); o4.w = cvt_pk_bf16(O[2 * u2 + 1][2] * inv, O[2 * u2 + 1][3] * inv); *(u32x4*)(op + 32 * u2) = o4; }
	v_mfma_f32_16x16x16_bf16 v[58:61], v[120:121], v[128:129], v[62:65]
	ds_read_b64_tr_b16 v[120:121], v132 offset:36864
	v_exp_f32_e32 v112, v112
	v_exp_f32_e32 v113, v113
	v_exp_f32_e32 v114, v114
	s_waitcnt lgkmcnt(2)
	v_mfma_f32_16x16x16_bf16 v[62:65], v[130:131], v[128:129], v[66:69]
	ds_read_b64_tr_b16 v[116:117], v132 offset:36928
	ds_read_b64_tr_b16 v[128:129], v132 offset:36936
	v_exp_f32_e32 v115, v115
	v_pk_add_f32 v[118:119], v[112:113], v[122:123]
	v_add_u32_e32 v122, v144, v105
	s_waitcnt lgkmcnt(2)
	v_mfma_f32_16x16x16_bf16 v[66:69], v[120:121], v[126:127], v[70:73]
	ds_read_b64_tr_b16 v[120:121], v122 offset:36872
	v_mfma_f32_16x16x16_bf16 v[70:73], v[124:125], v[126:127], v[74:77]
	s_nop 2
	v_add_f32_e64 v74, v114, v78
	v_add_f32_e64 v75, v115, v79
	v_pk_add_f32 v[76:77], v[54:55], v[44:45]
	v_pk_add_f32 v[78:79], v[56:57], v[42:43]
	s_waitcnt lgkmcnt(2)
	v_mfma_f32_16x16x16_bf16 v[54:57], v[116:117], v[126:127], v[58:61]
	ds_read_b64_tr_b16 v[116:117], v122 offset:36864
	v_cvt_pk_bf16_f32 v114, v114, v115
	v_cvt_pk_bf16_f32 v115, v112, v113
	ds_read_b64_tr_b16 v[112:113], v122 offset:36928
	ds_read_b64_tr_b16 v[122:123], v122 offset:36936
	s_waitcnt lgkmcnt(4)
	v_mfma_f32_16x16x16_bf16 v[58:61], v[128:129], v[126:127], v[62:65]
	v_exp_f32_e32 v76, v76
	v_exp_f32_e32 v77, v77
	v_exp_f32_e32 v78, v78
	s_waitcnt lgkmcnt(2)
	v_mfma_f32_16x16x16_bf16 v[62:65], v[116:117], v[114:115], v[66:69]
	v_exp_f32_e32 v79, v79
	v_pk_add_f32 v[116:117], v[76:77], v[118:119]
	v_mfma_f32_16x16x16_bf16 v[66:69], v[120:121], v[114:115], v[70:73]
	s_nop 2
	v_add_f32_e64 v70, v42, v46
	v_add_f32_e64 v71, v43, v47
	s_waitcnt lgkmcnt(1)
	v_mfma_f32_16x16x16_bf16 v[42:45], v[112:113], v[114:115], v[54:57]
	v_exp_f32_e32 v72, v48
	v_exp_f32_e32 v73, v49
	v_exp_f32_e32 v70, v70
	v_add_u32_e32 v56, v144, v106
	ds_read_b64_tr_b16 v[54:55], v56 offset:36864
	s_waitcnt lgkmcnt(1)
	v_mfma_f32_16x16x16_bf16 v[46:49], v[122:123], v[114:115], v[58:61]
	v_exp_f32_e32 v71, v71
	v_cvt_pk_bf16_f32 v112, v78, v79
	v_cvt_pk_bf16_f32 v113, v76, v77
	ds_read_b64_tr_b16 v[58:59], v56 offset:36872
	ds_read_b64_tr_b16 v[76:77], v56 offset:36928
	ds_read_b64_tr_b16 v[114:115], v56 offset:36936
	s_waitcnt lgkmcnt(3)
	v_mfma_f32_16x16x16_bf16 v[54:57], v[54:55], v[112:113], v[62:65]
	s_nop 2
	v_add_f32_e64 v62, v78, v74
	v_add_f32_e64 v63, v79, v75
	v_pk_add_f32 v[64:65], v[72:73], v[116:117]
	v_pk_add_f32 v[62:63], v[70:71], v[62:63]
	v_add_u32_e32 v74, v144, v107
	s_waitcnt lgkmcnt(2)
	v_mfma_f32_16x16x16_bf16 v[58:61], v[58:59], v[112:113], v[66:69]
	s_nop 2
	v_pk_mov_b32 v[66:67], v[62:63], v[64:65] op_sel:[1,0]
	v_mov_b32_e32 v63, v65
	ds_read_b64_tr_b16 v[64:65], v74 offset:36864
	v_pk_add_f32 v[62:63], v[66:67], v[62:63]
	v_cvt_pk_bf16_f32 v66, v70, v71
	v_add_f32_e32 v75, v62, v63
	v_cvt_pk_bf16_f32 v67, v72, v73
	s_waitcnt lgkmcnt(2)
	v_mfma_f32_16x16x16_bf16 v[42:45], v[76:77], v[112:113], v[42:45]
	ds_read_b64_tr_b16 v[62:63], v74 offset:36872
	ds_read_b64_tr_b16 v[68:69], v74 offset:36928
	ds_read_b64_tr_b16 v[70:71], v74 offset:36936
	s_waitcnt lgkmcnt(3)
	v_mfma_f32_16x16x16_bf16 v[54:57], v[64:65], v[66:67], v[54:57]
	ds_bpermute_b32 v64, v142, v75
	s_waitcnt lgkmcnt(0)
	v_add_f32_e32 v72, v75, v64
	ds_bpermute_b32 v73, v143, v72
	v_mfma_f32_16x16x16_bf16 v[58:61], v[62:63], v[66:67], v[58:61]
	v_mfma_f32_16x16x16_bf16 v[62:65], v[68:69], v[66:67], v[42:45]
	s_waitcnt lgkmcnt(0)
	s_nop 1
	v_add_f32_e32 v43, v72, v73
	v_div_scale_f32 v68, s[64:65], v43, v43, 1.0
	v_mfma_f32_16x16x16_bf16 v[46:49], v[114:115], v[112:113], v[46:49]
	v_rcp_f32_e32 v69, v68
	v_lshlrev_b32_e32 v42, s35, v110
	s_ashr_i32 s35, s34, 31
	v_mfma_f32_16x16x16_bf16 v[44:47], v[70:71], v[66:67], v[46:49]
	s_lshl_b64 s[64:65], s[26:27], 16
	s_lshl_b64 s[34:35], s[34:35], 12
	s_ashr_i32 s26, s31, 31
	s_nop 0
	v_fma_f32 v48, -v68, v69, 1.0
	v_fmac_f32_e32 v69, v48, v69
	v_div_scale_f32 v48, vcc, 1.0, v43, 1.0
	v_mul_f32_e32 v49, v48, v69
	s_add_u32 s31, s34, s31
	v_fma_f32 v66, -v68, v49, v48
	s_addc_u32 s26, s35, s26
	v_fmac_f32_e32 v49, v66, v69
	s_add_u32 s34, s31, s64
	v_fma_f32 v48, -v68, v49, v48
	s_addc_u32 s35, s26, s65
	v_div_fmas_f32 v48, v48, v69, v49
	s_lshl_b32 s26, s30, 7
	s_lshl_b64 s[64:65], s[34:35], 10
	v_div_fixup_f32 v48, v48, v43, 1.0
	s_add_u32 s31, s24, s64
	v_lshl_or_b32 v49, v42, 10, v82
	s_addc_u32 s37, s25, s65
	v_pk_mul_f32 v[54:55], v[48:49], v[54:55] op_sel_hi:[0,1]
	v_pk_mul_f32 v[56:57], v[48:49], v[56:57] op_sel_hi:[0,1]
	s_add_u32 s64, s31, s26
	v_cvt_pk_bf16_f32 v54, v54, v55
	v_cvt_pk_bf16_f32 v55, v56, v57
	v_pk_mul_f32 v[56:57], v[48:49], v[58:59] op_sel_hi:[0,1]
	v_pk_mul_f32 v[58:59], v[48:49], v[60:61] op_sel_hi:[0,1]
	s_addc_u32 s65, s37, 0
	v_cvt_pk_bf16_f32 v56, v56, v57
	v_cvt_pk_bf16_f32 v57, v58, v59
	global_store_dwordx4 v49, v[54:57], s[64:65]
	v_pk_mul_f32 v[44:45], v[48:49], v[44:45] op_sel_hi:[0,1]
	s_nop 0
	v_pk_mul_f32 v[54:55], v[48:49], v[62:63] op_sel_hi:[0,1]
	v_pk_mul_f32 v[56:57], v[48:49], v[64:65] op_sel_hi:[0,1]
	v_cvt_pk_bf16_f32 v54, v54, v55
	v_cvt_pk_bf16_f32 v55, v56, v57
	v_cvt_pk_bf16_f32 v56, v44, v45
	v_pk_mul_f32 v[44:45], v[48:49], v[46:47] op_sel_hi:[0,1]
	v_cvt_pk_bf16_f32 v57, v44, v45
	global_store_dwordx4 v49, v[54:57], s[64:65] offset:64
	s_cmp_eq_u32 s95, 0
	s_cbranch_scc1 .Lcva_skip_l
; #define LAS __attribute__((address_space(3)))
; __device__ __forceinline__ void titem_finish(const TItem& t, int lane, const LAS unsigned char* buf) {
;     const int nblk = t.N / 32, kb = t.item / nblk, nb = t.item % nblk, k0 = 64 * kb, n0 = 32 * nb;
;     const int d0 = t.gmode == 0 ? n0 : ((n0 >> 7) * 256 + (n0 & 127) + (t.gmode == 2 ? 128 : 0));
;     const int c = lane & 7;
;     const LAS float* sb = (const LAS float*)buf;
;     float v[4][8];
;     const float wsc = t.scale;
; #pragma unroll
;     for (int j = 0; j < 4; ++j) { const int n = (lane >> 3) + 8 * j; const LAS float* s = sb + (8 * c) * 32 + 4 * ((n >> 2) ^ c) + (n & 3);
; #pragma unroll
;         for (int q = 0; q < 8; ++q) v[j][q] = s[32 * q] * wsc; }
;     if (t.f8) {
; #pragma unroll
;         for (int j = 0; j < 4; ++j) { const int n = (lane >> 3) + 8 * j;
;             int w0 = __builtin_amdgcn_cvt_pk_fp8_f32(v[j][0], v[j][1], 0, false); w0 = __builtin_amdgcn_cvt_pk_fp8_f32(v[j][2], v[j][3], w0, true);
;             int w1 = __builtin_amdgcn_cvt_pk_fp8_f32(v[j][4], v[j][5], 0, false); w1 = __builtin_amdgcn_cvt_pk_fp8_f32(v[j][6], v[j][7], w1, true);
;             u32x2 o; o.x = (unsigned)w0; o.y = (unsigned)w1;
;             __builtin_nontemporal_store(o, (u32x2*)((unsigned char*)t.WT + (size_t)(d0 + n) * t.K + k0 + 8 * c)); }
; __device__ __forceinline__ void phase_attn(Frame& F) {
;     ...
;         if (fq == 0) *(float*)((char*)lse + (((size_t)cu.dsel * NTOK + (size_t)cu.b * SEQ + cu.r) * 8 + cu.h) * 4 + qrow * 32u) = mx + __builtin_amdgcn_logf(l);
;         cu = nu; buf ^= 1;
	s_waitcnt vmcnt(12)
	v_pk_mul_f32 v[168:169], v[168:169], s[94:95] op_sel_hi:[1,0]
	v_pk_mul_f32 v[170:171], v[170:171], s[94:95] op_sel_hi:[1,0]
	v_pk_mul_f32 v[172:173], v[172:173], s[94:95] op_sel_hi:[1,0]
	v_pk_mul_f32 v[174:175], v[174:175], s[94:95] op_sel_hi:[1,0]
	v_pk_mul_f32 v[176:177], v[176:177], s[94:95] op_sel_hi:[1,0]
	v_pk_mul_f32 v[178:179], v[178:179], s[94:95] op_sel_hi:[1,0]
	v_pk_mul_f32 v[180:181], v[180:181], s[94:95] op_sel_hi:[1,0]
	v_pk_mul_f32 v[182:183], v[182:183], s[94:95] op_sel_hi:[1,0]
	v_pk_mul_f32 v[184:185], v[184:185], s[94:95] op_sel_hi:[1,0]
	v_pk_mul_f32 v[186:187], v[186:187], s[94:95] op_sel_hi:[1,0]
	v_pk_mul_f32 v[188:189], v[188:189], s[94:95] op_sel_hi:[1,0]
	v_pk_mul_f32 v[190:191], v[190:191], s[94:95] op_sel_hi:[1,0]
	v_pk_mul_f32 v[192:193], v[192:193], s[94:95] op_sel_hi:[1,0]
	v_pk_mul_f32 v[194:195], v[194:195], s[94:95] op_sel_hi:[1,0]
	v_pk_mul_f32 v[196:197], v[196:197], s[94:95] op_sel_hi:[1,0]
	v_pk_mul_f32 v[198:199], v[198:199], s[94:95] op_sel_hi:[1,0]
	v_pk_mul_f32 v[200:201], v[200:201], s[94:95] op_sel_hi:[1,0]
	v_pk_mul_f32 v[202:203], v[202:203], s[94:95] op_sel_hi:[1,0]
	v_pk_mul_f32 v[204:205], v[204:205], s[94:95] op_sel_hi:[1,0]
	v_pk_mul_f32 v[206:207], v[206:207], s[94:95] op_sel_hi:[1,0]
	v_pk_mul_f32 v[208:209], v[208:209], s[94:95] op_sel_hi:[1,0]
	v_pk_mul_f32 v[210:211], v[210:211], s[94:95] op_sel_hi:[1,0]
	v_pk_mul_f32 v[212:213], v[212:213], s[94:95] op_sel_hi:[1,0]
	v_pk_mul_f32 v[214:215], v[214:215], s[94:95] op_sel_hi:[1,0]
	v_pk_mul_f32 v[216:217], v[216:217], s[94:95] op_sel_hi:[1,0]
	v_pk_mul_f32 v[218:219], v[218:219], s[94:95] op_sel_hi:[1,0]
	v_pk_mul_f32 v[220:221], v[220:221], s[94:95] op_sel_hi:[1,0]
	v_pk_mul_f32 v[222:223], v[222:223], s[94:95] op_sel_hi:[1,0]
	v_pk_mul_f32 v[224:225], v[224:225], s[94:95] op_sel_hi:[1,0]
	v_pk_mul_f32 v[226:227], v[226:227], s[94:95] op_sel_hi:[1,0]
	v_pk_mul_f32 v[228:229], v[228:229], s[94:95] op_sel_hi:[1,0]
	v_pk_mul_f32 v[230:231], v[230:231], s[94:95] op_sel_hi:[1,0]
	s_lshr_b32 s99, s95, 2
	v_lshlrev_b32_e32 v250, 4, v248
	v_cvt_pk_fp8_f32 v232, v168, v172
	v_cvt_pk_fp8_f32 v233, v184, v188
	v_cvt_pk_fp8_f32 v234, v200, v204
	v_cvt_pk_fp8_f32 v235, v216, v220
	v_cvt_pk_fp8_f32 v236, v169, v173
	v_cvt_pk_fp8_f32 v237, v185, v189
	v_cvt_pk_fp8_f32 v238, v201, v205
	v_cvt_pk_fp8_f32 v239, v217, v221
	v_cvt_pk_fp8_f32 v240, v170, v174
	v_cvt_pk_fp8_f32 v241, v186, v190
	v_cvt_pk_fp8_f32 v242, v202, v206
	v_cvt_pk_fp8_f32 v243, v218, v222
	v_cvt_pk_fp8_f32 v244, v171, v175
	v_cvt_pk_fp8_f32 v245, v187, v191
	v_cvt_pk_fp8_f32 v246, v203, v207
	v_cvt_pk_fp8_f32 v247, v219, v223
	v_mad_u32_u24 v250, v249, s99, v250
	v_add_u32_e32 v251, s95, v250
	v_add_u32_e32 v254, s95, v251
	v_add_u32_e32 v255, s95, v254
	v_cvt_pk_fp8_f32 v232, v176, v180 op_sel:[0,0,1]
	v_cvt_pk_fp8_f32 v233, v192, v196 op_sel:[0,0,1]
	v_cvt_pk_fp8_f32 v234, v208, v212 op_sel:[0,0,1]
	v_cvt_pk_fp8_f32 v235, v224, v228 op_sel:[0,0,1]
	v_cvt_pk_fp8_f32 v236, v177, v181 op_sel:[0,0,1]
	v_cvt_pk_fp8_f32 v237, v193, v197 op_sel:[0,0,1]
	v_cvt_pk_fp8_f32 v238, v209, v213 op_sel:[0,0,1]
	v_cvt_pk_fp8_f32 v239, v225, v229 op_sel:[0,0,1]
	v_cvt_pk_fp8_f32 v240, v178, v182 op_sel:[0,0,1]
	v_cvt_pk_fp8_f32 v241, v194, v198 op_sel:[0,0,1]
	v_cvt_pk_fp8_f32 v242, v210, v214 op_sel:[0,0,1]
	v_cvt_pk_fp8_f32 v243, v226, v230 op_sel:[0,0,1]
	v_cvt_pk_fp8_f32 v244, v179, v183 op_sel:[0,0,1]
	v_cvt_pk_fp8_f32 v245, v195, v199 op_sel:[0,0,1]
	v_cvt_pk_fp8_f32 v246, v211, v215 op_sel:[0,0,1]
	v_cvt_pk_fp8_f32 v247, v227, v231 op_sel:[0,0,1]
	global_store_dwordx4 v250, v[232:235], s[92:93] nt
	global_store_dwordx4 v251, v[236:239], s[92:93] nt
	global_store_dwordx4 v254, v[240:243], s[92:93] nt
	global_store_dwordx4 v255, v[244:247], s[92:93] nt
	s_mov_b32 s95, 0
.Lcva_skip_l:
	s_and_saveexec_b64 s[64:65], s[4:5]
	s_cbranch_execz .LBB0_303
	s_mov_b32 s31, s27
	v_log_f32_e32 v43, v43
	s_lshl_b64 s[34:35], s[34:35], 5
	s_lshl_b64 s[30:31], s[30:31], 2
	s_add_u32 s26, s67, s34
	s_addc_u32 s34, s68, s35
	s_add_u32 s30, s26, s30
	v_add_f32_e32 v43, v111, v43
	s_addc_u32 s31, s34, s31
	v_lshlrev_b32_e32 v42, 5, v42
	global_store_dword v42, v43, s[30:31]
	s_branch .LBB0_303
